# P6 LayerNorm rows and P2 gMLP statistics: serialised load-wait chains replaced by batched loads with counted waits; LN parameter copies straight-line
# speedup vs baseline: 1.0202x; 1.0107x over previous
.LBB0_334:
	v_lshl_add_u64 v[60:61], v[56:57], 0, s[74:75]
	v_add_co_u32_e32 v64, vcc, 0x39405000, v60
	s_add_u32 s74, s74, 0x200
	s_nop 0
	v_addc_co_u32_e32 v65, vcc, 0, v61, vcc
	global_load_dwordx4 v[192:195], v[64:65], off
	global_load_dwordx4 v[196:199], v[64:65], off offset:64
	global_load_dwordx4 v[200:203], v[64:65], off offset:128
	global_load_dwordx4 v[204:207], v[64:65], off offset:192
	global_load_dwordx4 v[208:211], v[64:65], off offset:256
	global_load_dwordx4 v[212:215], v[64:65], off offset:320
	global_load_dwordx4 v[216:219], v[64:65], off offset:384
	global_load_dwordx4 v[220:223], v[64:65], off offset:448
	s_addc_u32 s75, s75, 0
	s_cmpk_eq_i32 s74, 0x800
	s_waitcnt vmcnt(7)
	v_lshlrev_b32_e32 v66, 16, v192
	v_and_b32_e32 v60, 0xffff0000, v192
	v_lshlrev_b32_e32 v68, 16, v193
	v_and_b32_e32 v108, 0xffff0000, v193
	v_lshlrev_b32_e32 v110, 16, v194
	v_and_b32_e32 v62, 0xffff0000, v194
	v_lshlrev_b32_e32 v112, 16, v195
	v_and_b32_e32 v114, 0xffff0000, v195
	v_mul_f32_e32 v67, v66, v66
	v_mul_f32_e32 v61, v60, v60
	v_mul_f32_e32 v69, v68, v68
	v_mul_f32_e32 v109, v108, v108
	v_mul_f32_e32 v111, v110, v110
	v_mul_f32_e32 v63, v62, v62
	v_mul_f32_e32 v113, v112, v112
	v_mul_f32_e32 v115, v114, v114
	v_pk_add_f32 v[60:61], v[66:67], v[60:61]
	v_pk_add_f32 v[66:67], v[68:69], v[108:109]
	v_pk_add_f32 v[62:63], v[110:111], v[62:63]
	v_pk_add_f32 v[60:61], v[60:61], v[66:67]
	v_pk_add_f32 v[66:67], v[112:113], v[114:115]
	s_nop 0
	v_pk_add_f32 v[62:63], v[62:63], v[66:67]
	s_nop 0
	v_pk_add_f32 v[60:61], v[60:61], v[62:63]
	s_nop 0
	v_pk_add_f32 v[62:63], v[58:59], v[60:61]
	s_waitcnt vmcnt(6)
	v_lshlrev_b32_e32 v66, 16, v196
	v_and_b32_e32 v58, 0xffff0000, v196
	v_lshlrev_b32_e32 v68, 16, v197
	v_and_b32_e32 v108, 0xffff0000, v197
	v_lshlrev_b32_e32 v110, 16, v198
	v_and_b32_e32 v60, 0xffff0000, v198
	v_lshlrev_b32_e32 v112, 16, v199
	v_and_b32_e32 v114, 0xffff0000, v199
	v_mul_f32_e32 v67, v66, v66
	v_mul_f32_e32 v59, v58, v58
	v_mul_f32_e32 v69, v68, v68
	v_mul_f32_e32 v109, v108, v108
	v_mul_f32_e32 v111, v110, v110
	v_mul_f32_e32 v61, v60, v60
	v_mul_f32_e32 v113, v112, v112
	v_mul_f32_e32 v115, v114, v114
	v_pk_add_f32 v[58:59], v[66:67], v[58:59]
	v_pk_add_f32 v[66:67], v[68:69], v[108:109]
	v_pk_add_f32 v[60:61], v[110:111], v[60:61]
	v_pk_add_f32 v[58:59], v[58:59], v[66:67]
	v_pk_add_f32 v[66:67], v[112:113], v[114:115]
	s_nop 0
	v_pk_add_f32 v[60:61], v[60:61], v[66:67]
	s_nop 0
	v_pk_add_f32 v[58:59], v[58:59], v[60:61]
	s_nop 0
	v_pk_add_f32 v[62:63], v[62:63], v[58:59]
	s_waitcnt vmcnt(5)
	v_lshlrev_b32_e32 v66, 16, v200
	v_and_b32_e32 v58, 0xffff0000, v200
	v_lshlrev_b32_e32 v68, 16, v201
	v_and_b32_e32 v108, 0xffff0000, v201
	v_lshlrev_b32_e32 v110, 16, v202
	v_and_b32_e32 v60, 0xffff0000, v202
	v_lshlrev_b32_e32 v112, 16, v203
	v_and_b32_e32 v114, 0xffff0000, v203
	v_mul_f32_e32 v67, v66, v66
	v_mul_f32_e32 v59, v58, v58
	v_mul_f32_e32 v69, v68, v68
	v_mul_f32_e32 v109, v108, v108
	v_mul_f32_e32 v111, v110, v110
	v_mul_f32_e32 v61, v60, v60
	v_mul_f32_e32 v113, v112, v112
	v_mul_f32_e32 v115, v114, v114
	v_pk_add_f32 v[58:59], v[66:67], v[58:59]
	v_pk_add_f32 v[66:67], v[68:69], v[108:109]
	v_pk_add_f32 v[60:61], v[110:111], v[60:61]
	v_pk_add_f32 v[58:59], v[58:59], v[66:67]
	v_pk_add_f32 v[66:67], v[112:113], v[114:115]
	s_nop 0
	v_pk_add_f32 v[60:61], v[60:61], v[66:67]
	s_nop 0
	v_pk_add_f32 v[58:59], v[58:59], v[60:61]
	s_nop 0
	v_pk_add_f32 v[62:63], v[62:63], v[58:59]
	s_waitcnt vmcnt(4)
	v_lshlrev_b32_e32 v66, 16, v204
	v_and_b32_e32 v58, 0xffff0000, v204
	v_lshlrev_b32_e32 v68, 16, v205
	v_and_b32_e32 v108, 0xffff0000, v205
	v_lshlrev_b32_e32 v110, 16, v206
	v_and_b32_e32 v60, 0xffff0000, v206
	v_lshlrev_b32_e32 v112, 16, v207
	v_and_b32_e32 v114, 0xffff0000, v207
	v_mul_f32_e32 v67, v66, v66
	v_mul_f32_e32 v59, v58, v58
	v_mul_f32_e32 v69, v68, v68
	v_mul_f32_e32 v109, v108, v108
	v_mul_f32_e32 v111, v110, v110
	v_mul_f32_e32 v61, v60, v60
	v_mul_f32_e32 v113, v112, v112
	v_mul_f32_e32 v115, v114, v114
	v_pk_add_f32 v[58:59], v[66:67], v[58:59]
	v_pk_add_f32 v[66:67], v[68:69], v[108:109]
	v_pk_add_f32 v[60:61], v[110:111], v[60:61]
	v_pk_add_f32 v[58:59], v[58:59], v[66:67]
	v_pk_add_f32 v[66:67], v[112:113], v[114:115]
	s_nop 0
	v_pk_add_f32 v[60:61], v[60:61], v[66:67]
	s_nop 0
	v_pk_add_f32 v[58:59], v[58:59], v[60:61]
	s_nop 0
	v_pk_add_f32 v[62:63], v[62:63], v[58:59]
	s_waitcnt vmcnt(3)
	v_lshlrev_b32_e32 v66, 16, v208
	v_and_b32_e32 v58, 0xffff0000, v208
	v_lshlrev_b32_e32 v68, 16, v209
	v_and_b32_e32 v108, 0xffff0000, v209
	v_lshlrev_b32_e32 v110, 16, v210
	v_and_b32_e32 v60, 0xffff0000, v210
	v_lshlrev_b32_e32 v112, 16, v211
	v_and_b32_e32 v114, 0xffff0000, v211
	v_mul_f32_e32 v67, v66, v66
	v_mul_f32_e32 v59, v58, v58
	v_mul_f32_e32 v69, v68, v68
	v_mul_f32_e32 v109, v108, v108
	v_mul_f32_e32 v111, v110, v110
	v_mul_f32_e32 v61, v60, v60
	v_mul_f32_e32 v113, v112, v112
	v_mul_f32_e32 v115, v114, v114
	v_pk_add_f32 v[58:59], v[66:67], v[58:59]
	v_pk_add_f32 v[66:67], v[68:69], v[108:109]
	v_pk_add_f32 v[60:61], v[110:111], v[60:61]
	v_pk_add_f32 v[58:59], v[58:59], v[66:67]
	v_pk_add_f32 v[66:67], v[112:113], v[114:115]
	s_nop 0
	v_pk_add_f32 v[60:61], v[60:61], v[66:67]
	s_nop 0
	v_pk_add_f32 v[58:59], v[58:59], v[60:61]
	s_nop 0
	v_pk_add_f32 v[62:63], v[62:63], v[58:59]
	s_waitcnt vmcnt(2)
	v_lshlrev_b32_e32 v66, 16, v212
	v_and_b32_e32 v58, 0xffff0000, v212
	v_lshlrev_b32_e32 v68, 16, v213
	v_and_b32_e32 v108, 0xffff0000, v213
	v_lshlrev_b32_e32 v110, 16, v214
	v_and_b32_e32 v60, 0xffff0000, v214
	v_lshlrev_b32_e32 v112, 16, v215
	v_and_b32_e32 v114, 0xffff0000, v215
	v_mul_f32_e32 v67, v66, v66
	v_mul_f32_e32 v59, v58, v58
	v_mul_f32_e32 v69, v68, v68
	v_mul_f32_e32 v109, v108, v108
	v_mul_f32_e32 v111, v110, v110
	v_mul_f32_e32 v61, v60, v60
	v_mul_f32_e32 v113, v112, v112
	v_mul_f32_e32 v115, v114, v114
	v_pk_add_f32 v[58:59], v[66:67], v[58:59]
	v_pk_add_f32 v[66:67], v[68:69], v[108:109]
	v_pk_add_f32 v[60:61], v[110:111], v[60:61]
	v_pk_add_f32 v[58:59], v[58:59], v[66:67]
	v_pk_add_f32 v[66:67], v[112:113], v[114:115]
	s_nop 0
	v_pk_add_f32 v[60:61], v[60:61], v[66:67]
	s_nop 0
	v_pk_add_f32 v[58:59], v[58:59], v[60:61]
	s_nop 0
	v_pk_add_f32 v[62:63], v[62:63], v[58:59]
	s_waitcnt vmcnt(1)
	v_lshlrev_b32_e32 v66, 16, v216
	v_and_b32_e32 v58, 0xffff0000, v216
	v_lshlrev_b32_e32 v68, 16, v217
	v_and_b32_e32 v108, 0xffff0000, v217
	v_lshlrev_b32_e32 v110, 16, v218
	v_and_b32_e32 v60, 0xffff0000, v218
	v_lshlrev_b32_e32 v112, 16, v219
	v_and_b32_e32 v114, 0xffff0000, v219
	v_mul_f32_e32 v67, v66, v66
	v_mul_f32_e32 v59, v58, v58
	v_mul_f32_e32 v69, v68, v68
	v_mul_f32_e32 v109, v108, v108
	v_mul_f32_e32 v111, v110, v110
	v_mul_f32_e32 v61, v60, v60
	v_mul_f32_e32 v113, v112, v112
	v_mul_f32_e32 v115, v114, v114
	v_pk_add_f32 v[58:59], v[66:67], v[58:59]
	v_pk_add_f32 v[66:67], v[68:69], v[108:109]
	v_pk_add_f32 v[60:61], v[110:111], v[60:61]
	v_pk_add_f32 v[58:59], v[58:59], v[66:67]
	v_pk_add_f32 v[66:67], v[112:113], v[114:115]
	s_nop 0
	v_pk_add_f32 v[60:61], v[60:61], v[66:67]
	s_nop 0
	v_pk_add_f32 v[58:59], v[58:59], v[60:61]
	s_nop 0
	v_pk_add_f32 v[62:63], v[62:63], v[58:59]
	s_waitcnt vmcnt(0)
	v_lshlrev_b32_e32 v64, 16, v220
	v_and_b32_e32 v58, 0xffff0000, v220
	v_lshlrev_b32_e32 v66, 16, v221
	v_and_b32_e32 v68, 0xffff0000, v221
	v_lshlrev_b32_e32 v108, 16, v222
	v_and_b32_e32 v60, 0xffff0000, v222
	v_lshlrev_b32_e32 v110, 16, v223
	v_and_b32_e32 v112, 0xffff0000, v223
	v_mul_f32_e32 v65, v64, v64
	v_mul_f32_e32 v59, v58, v58
	v_mul_f32_e32 v67, v66, v66
	v_mul_f32_e32 v69, v68, v68
	v_mul_f32_e32 v109, v108, v108
	v_mul_f32_e32 v61, v60, v60
	v_mul_f32_e32 v111, v110, v110
	v_mul_f32_e32 v113, v112, v112
	v_pk_add_f32 v[58:59], v[64:65], v[58:59]
	v_pk_add_f32 v[64:65], v[66:67], v[68:69]
	v_pk_add_f32 v[60:61], v[108:109], v[60:61]
	v_pk_add_f32 v[58:59], v[58:59], v[64:65]
	v_pk_add_f32 v[64:65], v[110:111], v[112:113]
	s_nop 0
	v_pk_add_f32 v[60:61], v[60:61], v[64:65]
	s_nop 0
	v_pk_add_f32 v[58:59], v[58:59], v[60:61]
	s_nop 0
	v_pk_add_f32 v[58:59], v[62:63], v[58:59]
	s_cbranch_scc0 .LBB0_334
	ds_bpermute_b32 v56, v83, v58
	ds_bpermute_b32 v57, v83, v59
	v_readlane_b32 s64, v254, 62
	v_readlane_b32 s65, v254, 63
	s_waitcnt lgkmcnt(1)
	v_add_f32_e32 v56, v58, v56
	s_waitcnt lgkmcnt(0)
	v_add_f32_e32 v58, v59, v57
	ds_bpermute_b32 v57, v140, v56
	ds_bpermute_b32 v59, v140, v58
	s_and_saveexec_b64 s[76:77], s[64:65]
	s_cbranch_execz .LBB0_337
	s_waitcnt lgkmcnt(1)
	v_add_f32_e32 v56, v56, v57
	v_mul_f32_e32 v56, 0x3a800000, v56
	s_waitcnt lgkmcnt(0)
	v_add_f32_e32 v58, v58, v59
	v_mul_f32_e32 v57, v56, v56
	s_mov_b32 s74, 0x3a800000
	v_fma_f32 v57, v58, s74, -v57
	v_max_f32_e32 v57, 0, v57
	v_add_f32_e32 v57, 0x3727c5ac, v57
	s_mov_b32 s74, 0xf800000
	v_mul_f32_e32 v58, 0x4f800000, v57
	v_cmp_gt_f32_e32 vcc, s74, v57
	ds_write_b32 v141, v56
	s_nop 0
	v_cndmask_b32_e32 v57, v57, v58, vcc
	v_sqrt_f32_e32 v58, v57
	s_nop 0
	v_add_u32_e32 v59, -1, v58
	v_fma_f32 v60, -v59, v58, v57
	v_cmp_ge_f32_e64 s[74:75], 0, v60
	v_add_u32_e32 v60, 1, v58
	s_nop 0
	v_cndmask_b32_e64 v59, v58, v59, s[74:75]
	v_fma_f32 v58, -v60, v58, v57
	v_cmp_lt_f32_e64 s[74:75], 0, v58
	s_nop 1
	v_cndmask_b32_e64 v58, v59, v60, s[74:75]
	v_mul_f32_e32 v59, 0x37800000, v58
	v_cndmask_b32_e32 v58, v58, v59, vcc
	v_cmp_class_f32_e32 vcc, v57, v155
	s_nop 1
	v_cndmask_b32_e32 v57, v58, v57, vcc
	v_div_scale_f32 v58, s[74:75], v57, v57, 1.0
	v_rcp_f32_e32 v59, v58
	s_nop 0
	v_fma_f32 v56, -v58, v59, 1.0
	v_fmac_f32_e32 v59, v56, v59
	v_div_scale_f32 v56, vcc, 1.0, v57, 1.0
	v_mul_f32_e32 v60, v56, v59
	v_fma_f32 v61, -v58, v60, v56
	v_fmac_f32_e32 v60, v61, v59
	v_fma_f32 v56, -v58, v60, v56
	v_div_fmas_f32 v56, v56, v59, v60
	v_div_fixup_f32 v56, v56, v57, 1.0
	ds_write_b32 v142, v56

.LBB0_701:
	s_and_saveexec_b64 s[12:13], s[82:83]
	global_load_dword v166, v[36:37], off
	s_mov_b64 exec, s[12:13]
	global_load_dword v8, v[4:5], off
	global_load_dword v9, v[2:3], off
	global_load_dword v160, v[4:5], off offset:2048
	global_load_dword v161, v[2:3], off offset:2048
	s_mov_b64 s[12:13], 0x1000
	v_add_u32_e32 v10, 0xffffe000, v6
	v_lshl_add_u64 v[4:5], v[4:5], 0, s[12:13]
	v_lshl_add_u64 v[2:3], v[2:3], 0, s[12:13]
	global_load_dword v162, v[4:5], off
	global_load_dword v163, v[2:3], off
	global_load_dword v164, v[4:5], off offset:2048
	global_load_dword v165, v[2:3], off offset:2048
	s_mov_b64 s[12:13], 0
	s_waitcnt vmcnt(6)
	ds_write_b32 v10, v8
	ds_write_b32 v6, v9
	s_waitcnt vmcnt(4)
	ds_write_b32 v10, v160 offset:2048
	ds_write_b32 v6, v161 offset:2048
	s_waitcnt vmcnt(2)
	ds_write_b32 v10, v162 offset:4096
	ds_write_b32 v6, v163 offset:4096
	s_waitcnt vmcnt(0)
	ds_write_b32 v10, v164 offset:6144
	ds_write_b32 v6, v165 offset:6144
	s_or_b64 exec, exec, s[12:13]
	s_waitcnt lgkmcnt(0)
	s_barrier
	s_and_saveexec_b64 s[12:13], s[82:83]
	s_cbranch_execz .LBB0_704
	ds_write_b32 v73, v166

.LBB0_706:
	v_lshl_add_u64 v[8:9], s[92:93], 0, v[4:5]
	v_add_co_u32_e32 v10, vcc, 0x69400000, v8
	v_mov_b32_e32 v144, 0
	s_nop 0
	v_addc_co_u32_e32 v11, vcc, 0, v9, vcc
	global_load_dwordx2 v[160:161], v[10:11], off
	v_add_co_u32_e32 v8, vcc, s43, v8
	v_lshl_add_u32 v144, v144, 2, v132
	s_nop 0
	v_addc_co_u32_e32 v9, vcc, 0, v9, vcc
	global_load_dwordx2 v[162:163], v[10:11], off offset:512
	global_load_dwordx2 v[164:165], v[10:11], off offset:1024
	global_load_dwordx2 v[166:167], v[10:11], off offset:1536
	global_load_dwordx2 v[168:169], v[10:11], off offset:2048
	global_load_dwordx2 v[170:171], v[10:11], off offset:2560
	global_load_dwordx2 v[172:173], v[10:11], off offset:3072
	global_load_dwordx2 v[174:175], v[10:11], off offset:3584
	s_waitcnt vmcnt(0)
	v_lshlrev_b32_e32 v6, 16, v160
	v_and_b32_e32 v7, 0xffff0000, v160
	v_lshlrev_b32_e32 v70, 16, v161
	v_and_b32_e32 v71, 0xffff0000, v161
	v_add_f32_e32 v12, v6, v7
	v_add_f32_e32 v13, v70, v71
	v_add_f32_e32 v12, v12, v13
	v_add_f32_e32 v14, 0, v12
	v_lshlrev_b32_e32 v66, 16, v162
	v_and_b32_e32 v67, 0xffff0000, v162
	v_lshlrev_b32_e32 v68, 16, v163
	v_and_b32_e32 v69, 0xffff0000, v163
	v_add_f32_e32 v12, v66, v67
	v_add_f32_e32 v13, v68, v69
	v_add_f32_e32 v12, v12, v13
	v_add_f32_e32 v14, v14, v12
	v_lshlrev_b32_e32 v64, 16, v164
	v_and_b32_e32 v65, 0xffff0000, v164
	v_lshlrev_b32_e32 v62, 16, v165
	v_and_b32_e32 v63, 0xffff0000, v165
	v_add_f32_e32 v12, v64, v65
	v_add_f32_e32 v13, v62, v63
	v_add_f32_e32 v12, v12, v13
	v_add_f32_e32 v14, v14, v12
	v_lshlrev_b32_e32 v58, 16, v166
	v_and_b32_e32 v59, 0xffff0000, v166
	v_lshlrev_b32_e32 v60, 16, v167
	v_and_b32_e32 v61, 0xffff0000, v167
	v_add_f32_e32 v12, v58, v59
	v_add_f32_e32 v13, v60, v61
	v_add_f32_e32 v12, v12, v13
	v_add_f32_e32 v14, v14, v12
	v_lshlrev_b32_e32 v56, 16, v168
	v_and_b32_e32 v57, 0xffff0000, v168
	v_lshlrev_b32_e32 v54, 16, v169
	v_and_b32_e32 v55, 0xffff0000, v169
	v_add_f32_e32 v12, v56, v57
	v_add_f32_e32 v13, v54, v55
	v_add_f32_e32 v12, v12, v13
	v_add_f32_e32 v14, v14, v12
	v_lshlrev_b32_e32 v32, 16, v170
	v_and_b32_e32 v33, 0xffff0000, v170
	v_lshlrev_b32_e32 v52, 16, v171
	v_and_b32_e32 v53, 0xffff0000, v171
	v_add_f32_e32 v12, v32, v33
	v_add_f32_e32 v13, v52, v53
	v_add_f32_e32 v12, v12, v13
	v_add_f32_e32 v14, v14, v12
	v_lshlrev_b32_e32 v30, 16, v172
	v_and_b32_e32 v31, 0xffff0000, v172
	v_lshlrev_b32_e32 v28, 16, v173
	v_and_b32_e32 v29, 0xffff0000, v173
	v_add_f32_e32 v12, v30, v31
	v_add_f32_e32 v13, v28, v29
	v_add_f32_e32 v12, v12, v13
	v_add_f32_e32 v12, v14, v12
	v_lshlrev_b32_e32 v24, 16, v174
	v_and_b32_e32 v25, 0xffff0000, v174
	v_lshlrev_b32_e32 v26, 16, v175
	v_and_b32_e32 v27, 0xffff0000, v175
	v_add_f32_e32 v10, v24, v25
	v_add_f32_e32 v11, v26, v27
	v_add_f32_e32 v10, v10, v11
	v_add_f32_e32 v34, v12, v10
	global_load_dwordx2 v[22:23], v[8:9], off
	global_load_dwordx2 v[20:21], v[8:9], off offset:512
	global_load_dwordx2 v[18:19], v[8:9], off offset:1024
	global_load_dwordx2 v[16:17], v[8:9], off offset:1536
	global_load_dwordx2 v[14:15], v[8:9], off offset:2048
	global_load_dwordx2 v[12:13], v[8:9], off offset:2560
	global_load_dwordx2 v[10:11], v[8:9], off offset:3072
	s_nop 0
	global_load_dwordx2 v[8:9], v[8:9], off offset:3584
	v_add_f32_dpp v34, v34, v34 quad_perm:[1,0,3,2] row_mask:0xf bank_mask:0xf bound_ctrl:1
	s_nop 1
	v_add_f32_dpp v34, v34, v34 quad_perm:[2,3,0,1] row_mask:0xf bank_mask:0xf bound_ctrl:1
	s_nop 1
	v_add_f32_dpp v34, v34, v34 row_half_mirror row_mask:0xf bank_mask:0xf bound_ctrl:1
	s_nop 1
	v_add_f32_dpp v34, v34, v34 row_mirror row_mask:0xf bank_mask:0xf bound_ctrl:1
	v_mov_b32_e32 v145, v34
	s_nop 1
	v_permlane16_swap_b32_e32 v34, v145
	v_add_f32_e32 v34, v34, v145
	v_mov_b32_e32 v145, v34
	s_nop 1
	v_permlane32_swap_b32_e32 v34, v145
	v_add_f32_e32 v145, v34, v145
	v_fmac_f32_e32 v71, 0xba000000, v145
	v_fmac_f32_e32 v7, 0xba000000, v145
	v_fmac_f32_e32 v70, 0xba000000, v145
	v_fmac_f32_e32 v6, 0xba000000, v145
	v_mul_f32_e32 v34, v7, v7
	v_mul_f32_e32 v146, v71, v71
	v_fmac_f32_e32 v34, v6, v6
	v_fmac_f32_e32 v146, v70, v70
	v_fmac_f32_e32 v69, 0xba000000, v145
	v_fmac_f32_e32 v67, 0xba000000, v145
	v_add_f32_e32 v34, v34, v146
	v_fmac_f32_e32 v68, 0xba000000, v145
	v_fmac_f32_e32 v66, 0xba000000, v145
	v_mul_f32_e32 v146, v67, v67
	v_mul_f32_e32 v147, v69, v69
	v_fmac_f32_e32 v146, v66, v66
	v_fmac_f32_e32 v147, v68, v68
	v_add_f32_e32 v146, v146, v147
	v_fmac_f32_e32 v63, 0xba000000, v145
	v_fmac_f32_e32 v65, 0xba000000, v145
	v_add_f32_e32 v34, v34, v146
	v_fmac_f32_e32 v62, 0xba000000, v145
	v_fmac_f32_e32 v64, 0xba000000, v145
	v_mul_f32_e32 v146, v65, v65
	v_mul_f32_e32 v147, v63, v63
	v_fmac_f32_e32 v146, v64, v64
	v_fmac_f32_e32 v147, v62, v62
	v_add_f32_e32 v146, v146, v147
	v_fmac_f32_e32 v61, 0xba000000, v145
	v_fmac_f32_e32 v59, 0xba000000, v145
	v_add_f32_e32 v34, v146, v34
	v_fmac_f32_e32 v60, 0xba000000, v145
	v_fmac_f32_e32 v58, 0xba000000, v145
	v_mul_f32_e32 v146, v59, v59
	v_mul_f32_e32 v147, v61, v61
	v_fmac_f32_e32 v146, v58, v58
	v_fmac_f32_e32 v147, v60, v60
	v_add_f32_e32 v146, v146, v147
	v_fmac_f32_e32 v55, 0xba000000, v145
	v_fmac_f32_e32 v57, 0xba000000, v145
	v_add_f32_e32 v34, v146, v34
	v_fmac_f32_e32 v54, 0xba000000, v145
	v_fmac_f32_e32 v56, 0xba000000, v145
	v_mul_f32_e32 v146, v57, v57
	v_mul_f32_e32 v147, v55, v55
	v_fmac_f32_e32 v146, v56, v56
	v_fmac_f32_e32 v147, v54, v54
	v_add_f32_e32 v146, v146, v147
	v_fmac_f32_e32 v53, 0xba000000, v145
	v_fmac_f32_e32 v33, 0xba000000, v145
	v_add_f32_e32 v34, v146, v34
	v_fmac_f32_e32 v52, 0xba000000, v145
	v_fmac_f32_e32 v32, 0xba000000, v145
	v_mul_f32_e32 v146, v33, v33
	v_mul_f32_e32 v147, v53, v53
	v_fmac_f32_e32 v146, v32, v32
	v_fmac_f32_e32 v147, v52, v52
	v_add_f32_e32 v146, v146, v147
	v_fmac_f32_e32 v29, 0xba000000, v145
	v_fmac_f32_e32 v31, 0xba000000, v145
	v_add_f32_e32 v34, v146, v34
	v_fmac_f32_e32 v28, 0xba000000, v145
	v_fmac_f32_e32 v30, 0xba000000, v145
	v_mul_f32_e32 v146, v31, v31
	v_mul_f32_e32 v147, v29, v29
	v_fmac_f32_e32 v146, v30, v30
	v_fmac_f32_e32 v147, v28, v28
	v_add_f32_e32 v146, v146, v147
	v_fmac_f32_e32 v27, 0xba000000, v145
	v_fmac_f32_e32 v25, 0xba000000, v145
	v_add_f32_e32 v34, v146, v34
	v_fmac_f32_e32 v26, 0xba000000, v145
	v_fmac_f32_e32 v24, 0xba000000, v145
	v_mul_f32_e32 v146, v25, v25
	v_mul_f32_e32 v147, v27, v27
	v_fmac_f32_e32 v146, v24, v24
	v_fmac_f32_e32 v147, v26, v26
	v_add_f32_e32 v146, v146, v147
	v_add_f32_e32 v34, v146, v34
	s_nop 1
	v_add_f32_dpp v34, v34, v34 quad_perm:[1,0,3,2] row_mask:0xf bank_mask:0xf bound_ctrl:1
	s_nop 1
	v_add_f32_dpp v34, v34, v34 quad_perm:[2,3,0,1] row_mask:0xf bank_mask:0xf bound_ctrl:1
	s_nop 1
	v_add_f32_dpp v34, v34, v34 row_half_mirror row_mask:0xf bank_mask:0xf bound_ctrl:1
	s_nop 1
	v_add_f32_dpp v34, v34, v34 row_mirror row_mask:0xf bank_mask:0xf bound_ctrl:1
	v_mov_b32_e32 v146, v34
	s_nop 1
	v_permlane16_swap_b32_e32 v34, v146
	v_add_f32_e32 v34, v34, v146
	v_mov_b32_e32 v146, v34
	s_nop 1
	v_permlane32_swap_b32_e32 v34, v146
	v_add_f32_e32 v34, v34, v146
	v_fmamk_f32 v34, v34, 0x3a000000, v135
	v_cmp_gt_f32_e32 vcc, s44, v34
	v_mul_f32_e32 v146, 0x4f800000, v34
	s_nop 0
	v_cndmask_b32_e32 v34, v34, v146, vcc
	v_sqrt_f32_e32 v146, v34
	s_nop 0
	v_add_u32_e32 v147, -1, v146
	v_fma_f32 v148, -v147, v146, v34
	v_cmp_ge_f32_e64 s[12:13], 0, v148
	v_add_u32_e32 v148, 1, v146
	s_nop 0
	v_cndmask_b32_e64 v147, v146, v147, s[12:13]
	v_fma_f32 v146, -v148, v146, v34
	v_cmp_lt_f32_e64 s[12:13], 0, v146
	s_nop 1
	v_cndmask_b32_e64 v146, v147, v148, s[12:13]
	v_mul_f32_e32 v147, 0x37800000, v146
	v_cndmask_b32_e32 v146, v146, v147, vcc
	v_cmp_class_f32_e32 vcc, v34, v136
	s_nop 1
	v_cndmask_b32_e32 v34, v146, v34, vcc
	v_div_scale_f32 v146, s[12:13], v34, v34, 1.0
	v_rcp_f32_e32 v147, v146
	s_nop 0
	v_fma_f32 v148, -v146, v147, 1.0
	v_fmac_f32_e32 v147, v148, v147
	v_div_scale_f32 v148, vcc, 1.0, v34, 1.0
	v_mul_f32_e32 v149, v148, v147
	v_fma_f32 v150, -v146, v149, v148
	v_fmac_f32_e32 v149, v150, v147
	v_fma_f32 v146, -v146, v149, v148
	v_div_fmas_f32 v146, v146, v147, v149
	v_div_fixup_f32 v34, v146, v34, 1.0
	ds_read_b128 v[146:149], v144
	ds_read_b128 v[150:153], v144 offset:8192
	v_pk_mul_f32 v[6:7], v[6:7], v[34:35] op_sel_hi:[1,0]
	v_pk_mul_f32 v[70:71], v[70:71], v[34:35] op_sel_hi:[1,0]
	v_pk_mul_f32 v[66:67], v[66:67], v[34:35] op_sel_hi:[1,0]
	v_pk_mul_f32 v[68:69], v[68:69], v[34:35] op_sel_hi:[1,0]
	s_waitcnt lgkmcnt(0)
	v_pk_fma_f32 v[6:7], v[146:147], v[6:7], v[150:151]
	v_mov_b32_e32 v146, 0
	v_cvt_pk_fp8_f32 v146, v6, v7
	v_pk_fma_f32 v[70:71], v[148:149], v[70:71], v[152:153]
	v_lshl_add_u64 v[6:7], s[92:93], 0, v[2:3]
	v_pk_mul_f32 v[64:65], v[64:65], v[34:35] op_sel_hi:[1,0]
	v_cvt_pk_fp8_f32 v146, v70, v71 op_sel:[0,0,1]
	v_mov_b32_e32 v70, 0
	v_pk_mul_f32 v[62:63], v[62:63], v[34:35] op_sel_hi:[1,0]
	v_pk_mul_f32 v[58:59], v[58:59], v[34:35] op_sel_hi:[1,0]
	global_store_dword v[6:7], v146, off offset:-2048
	ds_read_b128 v[146:149], v144 offset:1024
	ds_read_b128 v[150:153], v144 offset:9216
	v_pk_mul_f32 v[60:61], v[60:61], v[34:35] op_sel_hi:[1,0]
	v_pk_mul_f32 v[56:57], v[56:57], v[34:35] op_sel_hi:[1,0]
	v_pk_mul_f32 v[54:55], v[54:55], v[34:35] op_sel_hi:[1,0]
	v_pk_mul_f32 v[32:33], v[32:33], v[34:35] op_sel_hi:[1,0]
	s_waitcnt lgkmcnt(0)
	v_pk_fma_f32 v[66:67], v[146:147], v[66:67], v[150:151]
	v_pk_fma_f32 v[68:69], v[148:149], v[68:69], v[152:153]
	v_cvt_pk_fp8_f32 v70, v66, v67
	v_pk_mul_f32 v[52:53], v[52:53], v[34:35] op_sel_hi:[1,0]
	v_pk_mul_f32 v[30:31], v[30:31], v[34:35] op_sel_hi:[1,0]
	v_pk_mul_f32 v[28:29], v[28:29], v[34:35] op_sel_hi:[1,0]
	v_cvt_pk_fp8_f32 v70, v68, v69 op_sel:[0,0,1]
	v_pk_mul_f32 v[24:25], v[24:25], v[34:35] op_sel_hi:[1,0]
	v_pk_mul_f32 v[26:27], v[26:27], v[34:35] op_sel_hi:[1,0]
	global_store_dword v[6:7], v70, off offset:-1792
	ds_read_b128 v[66:69], v144 offset:2048
	ds_read_b128 v[146:149], v144 offset:10240
	s_waitcnt lgkmcnt(0)
	v_pk_fma_f32 v[64:65], v[64:65], v[66:67], v[146:147]
	v_mov_b32_e32 v66, 0
	v_cvt_pk_fp8_f32 v66, v64, v65
	v_pk_fma_f32 v[62:63], v[62:63], v[68:69], v[148:149]
	s_nop 0
	v_cvt_pk_fp8_f32 v66, v62, v63 op_sel:[0,0,1]
	global_store_dword v[6:7], v66, off offset:-1536
	ds_read_b128 v[62:65], v144 offset:3072
	ds_read_b128 v[66:69], v144 offset:11264
	s_waitcnt lgkmcnt(0)
	v_pk_fma_f32 v[58:59], v[58:59], v[62:63], v[66:67]
	v_mov_b32_e32 v62, 0
	v_cvt_pk_fp8_f32 v62, v58, v59
	v_pk_fma_f32 v[60:61], v[60:61], v[64:65], v[68:69]
	s_nop 0
	v_cvt_pk_fp8_f32 v62, v60, v61 op_sel:[0,0,1]
	global_store_dword v[6:7], v62, off offset:-1280
	ds_read_b128 v[58:61], v144 offset:4096
	ds_read_b128 v[62:65], v144 offset:12288
	s_waitcnt lgkmcnt(0)
	v_pk_fma_f32 v[56:57], v[56:57], v[58:59], v[62:63]
	v_mov_b32_e32 v58, 0
	v_cvt_pk_fp8_f32 v58, v56, v57
	v_pk_fma_f32 v[54:55], v[54:55], v[60:61], v[64:65]
	s_nop 0
	v_cvt_pk_fp8_f32 v58, v54, v55 op_sel:[0,0,1]
	global_store_dword v[6:7], v58, off offset:-1024
	ds_read_b128 v[54:57], v144 offset:5120
	ds_read_b128 v[58:61], v144 offset:13312
	s_waitcnt lgkmcnt(0)
	v_pk_fma_f32 v[32:33], v[32:33], v[54:55], v[58:59]
	v_mov_b32_e32 v54, 0
	v_cvt_pk_fp8_f32 v54, v32, v33
	v_pk_fma_f32 v[52:53], v[52:53], v[56:57], v[60:61]
	v_mov_b32_e32 v32, 0
	v_cvt_pk_fp8_f32 v54, v52, v53 op_sel:[0,0,1]
	global_store_dword v[6:7], v54, off offset:-768
	ds_read_b128 v[52:55], v144 offset:6144
	ds_read_b128 v[56:59], v144 offset:14336
	s_waitcnt lgkmcnt(0)
	v_pk_fma_f32 v[30:31], v[30:31], v[52:53], v[56:57]
	s_nop 0
	v_cvt_pk_fp8_f32 v32, v30, v31
	v_pk_fma_f32 v[28:29], v[28:29], v[54:55], v[58:59]
	s_nop 0
	v_cvt_pk_fp8_f32 v32, v28, v29 op_sel:[0,0,1]
	global_store_dword v[6:7], v32, off offset:-512
	ds_read_b128 v[28:31], v144 offset:7168
	ds_read_b128 v[52:55], v144 offset:15360
	s_waitcnt lgkmcnt(0)
	v_pk_fma_f32 v[24:25], v[24:25], v[28:29], v[52:53]
	v_mov_b32_e32 v28, 0
	v_cvt_pk_fp8_f32 v28, v24, v25
	v_pk_fma_f32 v[26:27], v[26:27], v[30:31], v[54:55]
	s_nop 0
	v_cvt_pk_fp8_f32 v28, v26, v27 op_sel:[0,0,1]
	global_store_dword v[6:7], v28, off offset:-256
	s_and_saveexec_b64 s[12:13], s[8:9]
	s_cbranch_execz .LBB0_708
	s_add_i32 s70, s37, -8
	s_add_u32 s68, s92, s14
	v_mul_f32_e32 v24, 0x3a000000, v145
	s_addc_u32 s69, s93, s15
	v_mov_b32_e32 v25, v34
	v_mov_b32_e32 v26, s70
	ds_write_b64 v26, v[24:25]
	global_store_dwordx2 v137, v[24:25], s[68:69]

.LBB0_1202:
	global_load_dword v12, v[2:3], off
	global_load_dword v13, v[4:5], off
	global_load_dword v14, v[6:7], off
	global_load_dword v15, v[8:9], off
	global_load_dword v16, v[2:3], off offset:2048
	global_load_dword v17, v[4:5], off offset:2048
	global_load_dword v18, v[6:7], off offset:2048
	global_load_dword v19, v[8:9], off offset:2048
	s_mov_b64 s[2:3], 0x1000
	v_lshl_add_u64 v[2:3], v[2:3], 0, s[2:3]
	v_lshl_add_u64 v[4:5], v[4:5], 0, s[2:3]
	v_lshl_add_u64 v[6:7], v[6:7], 0, s[2:3]
	v_lshl_add_u64 v[8:9], v[8:9], 0, s[2:3]
	global_load_dword v20, v[2:3], off
	global_load_dword v21, v[4:5], off
	global_load_dword v22, v[6:7], off
	global_load_dword v23, v[8:9], off
	global_load_dword v24, v[2:3], off offset:2048
	global_load_dword v25, v[4:5], off offset:2048
	global_load_dword v26, v[6:7], off offset:2048
	global_load_dword v27, v[8:9], off offset:2048
	s_waitcnt vmcnt(12)
	ds_write2st64_b32 v11, v12, v13 offset1:32
	ds_write2st64_b32 v11, v14, v15 offset0:64 offset1:96
	s_waitcnt vmcnt(8)
	ds_write2st64_b32 v11, v16, v17 offset0:8 offset1:40
	ds_write2st64_b32 v11, v18, v19 offset0:72 offset1:104
	s_waitcnt vmcnt(4)
	ds_write2st64_b32 v11, v20, v21 offset0:16 offset1:48
	ds_write2st64_b32 v11, v22, v23 offset0:80 offset1:112
	s_waitcnt vmcnt(0)
	ds_write2st64_b32 v11, v24, v25 offset0:24 offset1:56
	ds_write2st64_b32 v11, v26, v27 offset0:88 offset1:120
	s_or_b64 exec, exec, s[0:1]
	s_ashr_i32 s97, s96, 31
	s_lshl_b64 s[0:1], s[96:97], 3
	s_add_u32 s4, s0, s86
	s_addc_u32 s5, s1, 0
	v_mov_b64_e32 v[2:3], 0x3fff
	v_cmp_gt_u64_e32 vcc, s[4:5], v[2:3]
	s_mov_b32 s87, 0
	s_mov_b32 s9, 3
	s_waitcnt lgkmcnt(0)
	s_barrier
	s_cbranch_vccnz .LBB0_1206
	s_ashr_i32 s91, s90, 31
	s_lshl_b64 s[6:7], s[90:91], 3
	v_lshrrev_b32_e32 v2, 2, v1
	v_mul_lo_u32 v2, s6, v2
	v_add_lshl_u32 v2, s4, v2, 2
	v_and_b32_e32 v3, 3, v0
	s_mov_b32 s0, 0xfffc
	v_and_or_b32 v2, v2, s0, v3
	v_lshlrev_b32_e32 v96, 2, v2
	v_mov_b32_e32 v97, 0
	v_lshl_add_u64 v[2:3], s[92:93], 0, v[96:97]
	v_add_co_u32_e32 v4, vcc, 0x100000, v2
	s_lshl_b64 s[2:3], s[96:97], 6
	s_nop 0
	v_addc_co_u32_e32 v5, vcc, 0, v3, vcc
	global_load_dword v8, v[4:5], off
	v_add_co_u32_e32 v2, vcc, 0x140000, v2
	s_lshl_b32 s12, s86, 3
	s_nop 0
	v_addc_co_u32_e32 v3, vcc, 0, v3, vcc
	global_load_dword v9, v[2:3], off
	s_add_u32 s21, s2, s12
	v_lshlrev_b32_e32 v4, 4, v0
	v_and_b32_e32 v5, 15, v0
	v_and_b32_e32 v0, 32, v0
	s_addc_u32 s22, s3, 0
	s_lshl_b64 s[12:13], s[90:91], 6
	s_lshl_b64 s[2:3], s[96:97], 15
	s_lshl_b64 s[14:15], s[86:87], 12
	v_lshrrev_b32_e32 v3, 4, v1
	v_lshlrev_b32_e32 v5, 5, v5
	v_lshrrev_b32_e32 v0, 1, v0
	s_add_u32 s2, s2, s14
	v_lshlrev_b32_e32 v10, 9, v3
	v_or3_b32 v0, s2, v5, v0
	s_addc_u32 s24, s3, s15
	v_or_b32_e32 v6, v10, v0
	s_mov_b64 s[18:19], 0x69400000
	s_movk_i32 s23, 0x200
	v_mov_b32_e32 v107, s24
	v_or_b32_e32 v106, 0xc00, v6
	v_lshl_add_u64 v[108:109], v[106:107], 0, s[18:19]
	v_and_or_b32 v106, v10, s23, v0
	s_lshl_b64 s[14:15], s[90:91], 15
	s_lshl_b64 s[2:3], s[96:97], 16
	s_lshl_b64 s[16:17], s[86:87], 13
	v_and_b32_e32 v96, 0xf0, v4
	s_add_u32 s2, s2, s16
	v_lshlrev_b32_e32 v2, 8, v3
	v_mov_b32_e32 v3, v97
	v_lshl_add_u64 v[4:5], s[92:93], 0, v[96:97]
	v_lshlrev_b32_e32 v11, 2, v96
	s_addc_u32 s3, s3, s17
	s_mov_b64 s[0:1], 0x8f400000
	v_or_b32_e32 v6, 0x400, v6
	v_mov_b32_e32 v7, s24
	v_lshl_add_u64 v[2:3], v[4:5], 0, v[2:3]
	v_and_or_b32 v96, v1, 48, v11
	s_add_u32 s16, s74, s2
	v_mov_b32_e32 v126, 0x79400000
	s_mov_b32 s11, 0x69400000
	s_mov_b32 s8, 0x3f9837f0
	s_mov_b32 s10, 0x3d800000
	v_mov_b32_e32 v127, 0x3727c5ac
	s_mov_b32 s20, 0xf800000
	v_mov_b32_e32 v128, 0x260
	v_mov_b32_e32 v99, v97
	v_mov_b32_e32 v101, v97
	v_mov_b32_e32 v103, v97
	v_mov_b32_e32 v105, v97
	v_lshl_add_u64 v[110:111], v[6:7], 0, s[18:19]
	v_lshl_add_u64 v[112:113], v[2:3], 0, s[0:1]
	v_add_u32_e32 v129, 0, v96
	s_addc_u32 s17, s75, s3
	s_lshl_b64 s[18:19], s[90:91], 16
	v_or_b32_e32 v98, 0x1000, v96
	v_or_b32_e32 v100, 0x1400, v96
	v_or_b32_e32 v102, 0x1800, v96
	v_or_b32_e32 v104, 0x1c00, v96
	v_mov_b64_e32 v[114:115], 0x4000
	s_waitcnt vmcnt(1)
	v_lshl_add_u32 v0, v8, 2, 0
	v_add_u32_e32 v0, 0x25100, v0
	ds_read_b32 v0, v0
	s_waitcnt vmcnt(0) lgkmcnt(0)
	v_lshl_add_u32 v130, v0, 8, v9
